# v28: as v27 but the static s_setprio 1 goes to waves 0-3 (other physical half)
# speedup vs baseline: 1.0001x; 1.0001x over previous
.LBB0_285:
	s_cmp_lt_i32 s72, 2
	s_cselect_b64 s[12:13], -1, 0
	s_and_b64 s[4:5], s[12:13], s[4:5]
	s_andn2_b64 vcc, exec, s[4:5]
	s_lshr_b32 s82, s97, 6
	s_cmp_ge_u32 s82, 4
	s_cbranch_scc1 .Lprio_done
	s_setprio 1

.LBB0_1736:
	s_setprio 1
	s_mov_b64 s[68:69], 0
